# P4 out-proj epilogue: residual loads pipelined 8 steps ahead in a VGPR ring; P6 query epilogue: row scales fetched up front (no per-step vmcnt(0) drain)
# baseline (speedup 1.0000x reference)
; #define GAS __attribute__((address_space(1)))
; #define SSD_DTLOAD(cc) do { if (wave == 0) { const unsigned _o = doff + (unsigned)(cc) * (128u * PP * 2u); \
;         dr0 = __uint_as_float((unsigned)*(const GAS unsigned short*)(projb + _o) << 16) + dtb; dr1 = __uint_as_float((unsigned)*(const GAS unsigned short*)(projb + (_o + 64u * PP * 2u)) << 16) + dtb; } } while (0)
; __device__ __forceinline__ void ssd_unit(LAS unsigned char* lds, int b, int h, const bf16* PROJ, const bf16* CONV, const float* dt_bias, const float* a_log, const float* ssd_d,
;                                          bf16* Y, float* SSQ, int tid, int wave, int lane) {
;     ...
;     const int g = h >> 3, pb = wave & 3, th = wave >> 2;
;     const float a_neg = -__expf(a_log[h]), dtb = dt_bias[h], Dh = ssd_d[h];
;     const size_t rowbase = (size_t)b * SEQ;
;     const GAS unsigned char* convb = (const GAS unsigned char*)CONV; const GAS unsigned char* projb = (const GAS unsigned char*)PROJ; GAS unsigned char* yb = (GAS unsigned char*)Y; GAS unsigned char* ssqb = (GAS unsigned char*)SSQ;
;     ...
;     f32x4 ST[8];
; #pragma unroll
;     for (int i = 0; i < 8; ++i) ST[i] = (f32x4){0.f, 0.f, 0.f, 0.f};
;     u32x4 pft[8], pfc[4]; float dr0 = 0.f, dr1 = 0.f;
;     ...
;     { SSD_ROLES(tid, lane) SSD_DTLOAD(0); SSD_PREFETCH(0); (void)r; (void)q; }
.LBB0_299:
	s_lshl_b32 s0, s1, 2
	s_and_b32 s6, s0, 28
	s_ashr_i32 s0, s1, 6
	s_add_i32 s6, s6, s0
	v_writelane_b32 v248, s1, 23
	s_bfe_u32 s0, s1, 0x30003
	s_lshl_b32 s1, s6, 3
	s_and_b32 s20, s1, 56
	s_or_b32 s5, s20, s0
	s_lshl_b32 s60, s5, 2
	v_readlane_b32 s44, v249, 41
	v_mov_b32_e32 v2, s60
	v_readlane_b32 s54, v249, 51
	v_readlane_b32 s55, v249, 52
	v_readlane_b32 s52, v249, 49
	v_readlane_b32 s53, v249, 50
	v_readlane_b32 s56, v249, 53
	v_readlane_b32 s57, v249, 54
	s_nop 0
	global_load_dword v34, v2, s[54:55]
	s_nop 0
	global_load_dword v148, v2, s[52:53]
	s_nop 0
	global_load_dword v151, v2, s[56:57]
	v_readlane_b32 s45, v249, 42
	v_readlane_b32 s46, v249, 43
	v_readlane_b32 s47, v249, 44
	v_readlane_b32 s48, v249, 45
	v_readlane_b32 s49, v249, 46
	v_readlane_b32 s50, v249, 47
	v_readlane_b32 s51, v249, 48
	v_readlane_b32 s58, v249, 55
	v_readlane_b32 s59, v249, 56
	s_mov_b64 s[0:1], exec
	v_readlane_b32 s42, v248, 5
	v_readlane_b32 s43, v248, 6
	s_and_b64 s[42:43], s[0:1], s[42:43]
	s_xor_b64 s[0:1], s[42:43], s[0:1]
	s_mov_b64 exec, s[42:43]
	s_lshl_b32 s21, s20, 4
	v_or_b32_e32 v35, s21, v168
	v_mov_b32_e32 v174, s21
	s_andn2_saveexec_b64 s[0:1], s[0:1]
	s_lshl_b32 s20, s20, 4
	v_lshl_or_b32 v35, s5, 6, v164
	v_mov_b32_e32 v174, s20
	s_or_b64 exec, exec, s[0:1]
	s_ashr_i32 s0, s6, 3
	s_ashr_i32 s1, s0, 31
	v_mov_b32_e32 v147, v146
	s_lshl_b64 s[80:81], s[0:1], 12
	v_cmp_ne_u32_e64 s[42:43], 1, v169
	s_andn2_b64 vcc, exec, s[24:25]
	v_mov_b64_e32 v[152:153], v[146:147]
	s_cbranch_vccnz .LBB0_305
	v_or_b32_e32 v2, s80, v182
	s_movk_i32 s0, 0x4900
	v_mul_lo_u32 v2, v2, s0
	v_or_b32_e32 v2, s5, v2
	v_lshlrev_b32_e32 v2, 1, v2
	v_add_u32_e32 v3, 0x9000, v2
	v_add_u32_e32 v2, 0x251000, v2
	global_load_ushort v3, v3, s[10:11]
	s_nop 0
	global_load_ushort v2, v2, s[10:11]
	s_waitcnt vmcnt(1)
	v_lshlrev_b32_e32 v3, 16, v3
	s_waitcnt vmcnt(0)
	v_lshlrev_b32_e32 v2, 16, v2
	v_pk_add_f32 v[152:153], v[148:149], v[2:3] op_sel_hi:[0,1]

; #define SSD_DTLOAD(cc) do { if (wave == 0) { const unsigned _o = doff + (unsigned)(cc) * (128u * PP * 2u); \
;         dr0 = __uint_as_float((unsigned)*(const GAS unsigned short*)(projb + _o) << 16) + dtb; dr1 = __uint_as_float((unsigned)*(const GAS unsigned short*)(projb + (_o + 64u * PP * 2u)) << 16) + dtb; } } while (0)
; __device__ __forceinline__ void ssd_unit(LAS unsigned char* lds, int b, int h, const bf16* PROJ, const bf16* CONV, const float* dt_bias, const float* a_log, const float* ssd_d,
;                                          bf16* Y, float* SSQ, int tid, int wave, int lane) {
;     ...
;     f32x4 ST[8];
; #pragma unroll
;     for (int i = 0; i < 8; ++i) ST[i] = (f32x4){0.f, 0.f, 0.f, 0.f};
;     u32x4 pft[8], pfc[4]; float dr0 = 0.f, dr1 = 0.f;
;     ...
;     { SSD_ROLES(tid, lane) SSD_DTLOAD(0); SSD_PREFETCH(0); (void)r; (void)q; }
;     if (wave == 0) ssd_dt_scan(smb, dr0, dr1, a_neg, lane);
;     for (int c = 0; c < SEQ / 128; ++c) {
;         const int t0 = c * 128, cn = c + 1 < SEQ / 128 ? c + 1 : c;
;         int tt = tid, ll = lane; asm volatile("" : "+v"(tt), "+v"(ll));
.LBB0_309:
	s_or_b32 s0, s5, 0x4800
	v_writelane_b32 v248, s0, 24
	s_lshl_b32 s0, s5, 6
	v_writelane_b32 v248, s0, 25
	s_add_u32 s0, s80, 0xffff80
	v_writelane_b32 v248, s0, 26
	v_readlane_b32 s0, v249, 34
	v_readlane_b32 s1, v249, 35
	v_writelane_b32 v248, s60, 27
	s_add_u32 s0, s0, s60
	s_addc_u32 s1, s1, 0
	v_writelane_b32 v248, s61, 28
	v_writelane_b32 v248, s0, 29
	v_mov_b32_e32 v46, 0
	v_or_b32_e32 v176, 0x1000, v174
	v_writelane_b32 v248, s1, 30
	s_lshl_b32 s0, s5, 7
	v_readlane_b32 s1, v248, 9
	s_or_b32 s20, s0, s1
	v_readlane_b32 s0, v248, 22
	s_waitcnt vmcnt(5)
	v_mov_b32_e32 v149, v148
	s_add_i32 s21, s37, s80
	s_add_i32 s6, s29, s80
	s_add_i32 s81, s0, s80
	s_mov_b32 s39, 0
	s_mov_b64 s[90:91], 0
	s_mov_b32 s5, 0
	v_mov_b32_e32 v47, v46
	v_mov_b32_e32 v48, v46
	v_mov_b32_e32 v49, v46
	v_mov_b32_e32 v62, v46
	v_mov_b32_e32 v63, v46
	v_mov_b32_e32 v64, v46
	v_mov_b32_e32 v65, v46
	v_mov_b32_e32 v34, v46
	v_mov_b32_e32 v35, v46
	v_mov_b32_e32 v36, v46
	v_mov_b32_e32 v37, v46
	v_mov_b32_e32 v38, v46
	v_mov_b32_e32 v39, v46
	v_mov_b32_e32 v40, v46
	v_mov_b32_e32 v41, v46
	v_mov_b32_e32 v42, v46
	v_mov_b32_e32 v43, v46
	v_mov_b32_e32 v44, v46
	v_mov_b32_e32 v45, v46
	v_mov_b32_e32 v50, v46
	v_mov_b32_e32 v51, v46
	v_mov_b32_e32 v52, v46
	v_mov_b32_e32 v53, v46
	v_mov_b32_e32 v54, v46
	v_mov_b32_e32 v55, v46
	v_mov_b32_e32 v56, v46
	v_mov_b32_e32 v57, v46
	v_mov_b32_e32 v58, v46
	v_mov_b32_e32 v59, v46
	v_mov_b32_e32 v60, v46
	v_mov_b32_e32 v61, v46
	s_branch .LBB0_311

; #define GAS __attribute__((address_space(1)))
; #define LAS __attribute__((address_space(3)))
; __device__ __forceinline__ void unpack8(const u32x4 v, float (&f)[8]) { f[0] = bflo(v.x); f[1] = bfhi(v.x); f[2] = bflo(v.y); f[3] = bfhi(v.y); f[4] = bflo(v.z); f[5] = bfhi(v.z); f[6] = bflo(v.w); f[7] = bfhi(v.w); }
; #define SSD_LBAR() do { asm volatile("s_waitcnt lgkmcnt(0)" ::: "memory"); __builtin_amdgcn_s_barrier(); asm volatile("" ::: "memory"); } while (0)
; __device__ __forceinline__ void ssd_unit(LAS unsigned char* lds, int b, int h, const bf16* PROJ, const bf16* CONV, const float* dt_bias, const float* a_log, const float* ssd_d,
;                                          bf16* Y, float* SSQ, int tid, int wave, int lane) {
;     ...
;         SSD_ROLES(tt, ll)
;         LAS float* dtv = smb + (c & 1) * 512; LAS float* acum = dtv + 128; LAS float* wend = dtv + 256; LAS float* eac = dtv + 384;
;         SSD_LBAR();
;         if (c > 0 && tt < 128) *(GAS float*)(ssqb + (unsigned)(((rowbase + t0 - 128 + tt) * NH + h) * 4)) = (ssqp[tt] + ssqp[128 + tt]) + (ssqp[256 + tt] + ssqp[384 + tt]);
; #pragma unroll
;         for (int k = 0; k < 4; ++k) *(LAS u32x4*)(lds + C_CM + sw256((tt >> 4) + 32 * k, tt & 15)) = pfc[k];
;         if (xitem || bitem) {
;             const LAS float* sc = xitem ? dtv : wend; const f32x4 sa = *(const LAS f32x4*)(sc + its * 8), sb2 = *(const LAS f32x4*)(sc + its * 8 + 4); const float s8[8] = {sa.x, sa.y, sa.z, sa.w, sb2.x, sb2.y, sb2.z, sb2.w};
;             float o[8][8];
; #pragma unroll
;             for (int i = 0; i < 8; ++i) { unpack8(pft[i], o[i]);
;                 if (xitem) *(LAS u32x4*)(lds + C_XB + sw128(its * 8 + i, icg)) = pft[i]; else *(LAS u32x4*)(lds + C_BM + sw256(its * 8 + i, icg)) = pft[i]; }
.LBB0_313:
	s_or_b64 exec, exec, s[0:1]
	v_ashrrev_i32_e32 v114, 4, v83
	v_add_u32_e32 v82, 0xffffff80, v83
	s_and_b32 s0, s39, 0x200
	v_xor_b32_e32 v87, v114, v83
	v_ashrrev_i32_e32 v84, 3, v83
	v_lshrrev_b32_e32 v85, 4, v82
	s_lshl_b32 s0, s0, 2
	v_lshlrev_b32_e32 v87, 4, v87
	v_cndmask_b32_e64 v82, v85, v84, s[46:47]
	s_add_i32 s88, s0, 0
	v_lshlrev_b32_e32 v86, 8, v114
	v_and_b32_e32 v87, 0xf0, v87
	s_movk_i32 s0, 0x180
	v_and_b32_e32 v115, 7, v83
	v_and_b32_e32 v117, 15, v83
	v_lshlrev_b32_e32 v116, 3, v82
	s_add_i32 s88, s88, 0x20200
	v_add3_u32 v86, 0, v87, v86
	v_cmp_gt_i32_e64 s[48:49], s0, v83
	s_waitcnt vmcnt(3)
	ds_write_b128 v86, v[66:69]
	s_waitcnt vmcnt(2)
	ds_write_b128 v86, v[70:73] offset:8192
	s_waitcnt vmcnt(1)
	ds_write_b128 v86, v[74:77] offset:16384
	s_waitcnt vmcnt(0)
	ds_write_b128 v86, v[78:81] offset:24576
	s_and_saveexec_b64 s[0:1], s[48:49]
	s_cbranch_execz .LBB0_333
	v_cndmask_b32_e64 v66, v173, 0, s[46:47]
	v_lshlrev_b32_e32 v67, 2, v116
	v_add3_u32 v66, s88, v66, v67
	ds_read_b128 v[70:73], v66
	ds_read_b128 v[66:69], v66 offset:16
	s_and_saveexec_b64 s[44:45], vcc
	s_xor_b64 s[44:45], exec, s[44:45]
	s_cbranch_execz .LBB0_316
	v_xor_b32_e32 v75, v116, v83
	v_lshlrev_b32_e32 v75, 4, v75
	v_lshlrev_b32_e32 v74, 11, v85
	v_and_b32_e32 v75, 0xf0, v75
	v_add3_u32 v74, 0, v75, v74
	ds_write_b128 v74, v[2:5] offset:32768

; #define SSD_DTLOAD(cc) do { if (wave == 0) { const unsigned _o = doff + (unsigned)(cc) * (128u * PP * 2u); \
;         dr0 = __uint_as_float((unsigned)*(const GAS unsigned short*)(projb + _o) << 16) + dtb; dr1 = __uint_as_float((unsigned)*(const GAS unsigned short*)(projb + (_o + 64u * PP * 2u)) << 16) + dtb; } } while (0)
; __device__ __forceinline__ void ssd_unit(LAS unsigned char* lds, int b, int h, const bf16* PROJ, const bf16* CONV, const float* dt_bias, const float* a_log, const float* ssd_d,
;                                          bf16* Y, float* SSQ, int tid, int wave, int lane) {
;     ...
;         SSD_DTLOAD(cn);
.LBB0_333:
	s_or_b64 exec, exec, s[0:1]
	s_add_i32 s5, s5, 1
	s_cmpk_lg_i32 s90, 0xf80
	s_cselect_b32 s89, s5, 31
	s_and_b64 vcc, exec, s[42:43]
	s_cbranch_vccnz .LBB0_335
	v_add_u32_e32 v66, s80, v150
	s_movk_i32 s0, 0x4900
	v_mul_lo_u32 v66, v66, s0
	v_readlane_b32 s0, v248, 24
	s_nop 1
	v_add_u32_e32 v66, s0, v66
	s_mul_i32 s0, s89, 0x490000
	v_lshl_add_u32 v66, v66, 1, s0
	v_add_u32_e32 v67, 0x248000, v66
	global_load_ushort v66, v66, s[10:11]
	s_nop 0
	global_load_ushort v68, v67, s[10:11]
	s_waitcnt vmcnt(1)
	v_lshlrev_b32_e32 v67, 16, v66
	s_waitcnt vmcnt(0)
	v_lshlrev_b32_e32 v66, 16, v68
	v_pk_add_f32 v[152:153], v[148:149], v[66:67]

; #define GAS __attribute__((address_space(1)))
; __device__ __forceinline__ void ssd_unit(LAS unsigned char* lds, int b, int h, const bf16* PROJ, const bf16* CONV, const float* dt_bias, const float* a_log, const float* ssd_d,
;                                          bf16* Y, float* SSQ, int tid, int wave, int lane) {
;     ...
;         u32x2 zv[4];
; #pragma unroll
;         for (int j = 0; j < 4; ++j) zv[j] = *(const GAS u32x2*)(projb + (unsigned)(((rowbase + t0 + 16 * (4 * th + j) + r) * PP + O_Z + h * 64 + 16 * pb + 4 * q) * 2));
;         SSD_PREFETCH(cn);
.LBB0_381:
	s_add_i32 s0, s6, s90
	v_add_u32_e32 v154, s20, v98
	v_add_u32_e32 v199, s0, v181
	v_mad_u64_u32 v[66:67], s[0:1], v199, s76, v[154:155]
	s_add_i32 s0, s81, s90
	s_nop 0
	v_add_u32_e32 v68, s0, v181
	v_add_u32_e32 v67, 0x92000, v66
	v_add_u32_e32 v70, 0x124000, v66
	v_mad_u64_u32 v[68:69], s[0:1], v68, s76, v[154:155]
	global_load_dwordx2 v[162:163], v66, s[10:11]
	global_load_dwordx2 v[160:161], v67, s[10:11]
	global_load_dwordx2 v[158:159], v70, s[10:11]
	global_load_dwordx2 v[156:157], v68, s[10:11]
	v_lshlrev_b32_e32 v66, 3, v117
	s_mul_i32 s89, s89, 0x180000
	s_and_saveexec_b64 s[0:1], s[48:49]
	s_cbranch_execz .LBB0_383
	v_readlane_b32 s48, v248, 25
	v_or_b32_e32 v3, v66, v176
	s_nop 0
	v_lshl_or_b32 v2, v115, 3, s48
	v_cndmask_b32_e64 v2, v3, v2, s[46:47]
	v_add_u32_e32 v3, s80, v116
	v_mad_u64_u32 v[2:3], s[46:47], v3, s4, v[2:3]
	v_lshl_add_u32 v26, v2, 1, s89
	v_add_u32_e32 v6, 0x3000, v26
	v_add_u32_e32 v10, 0x6000, v26
	v_add_u32_e32 v14, 0x9000, v26
	v_add_u32_e32 v18, 0xc000, v26
	v_add_u32_e32 v22, 0xf000, v26
	v_add_u32_e32 v27, 0x12000, v26
	v_add_u32_e32 v30, 0x15000, v26
	global_load_dwordx4 v[2:5], v26, s[8:9]
	s_nop 0
	global_load_dwordx4 v[6:9], v6, s[8:9]
	s_nop 0
	global_load_dwordx4 v[10:13], v10, s[8:9]
	s_nop 0
	global_load_dwordx4 v[14:17], v14, s[8:9]
	s_nop 0
	global_load_dwordx4 v[18:21], v18, s[8:9]
	s_nop 0
	global_load_dwordx4 v[22:25], v22, s[8:9]
	s_nop 0
	global_load_dwordx4 v[26:29], v27, s[8:9]
	s_nop 0
	global_load_dwordx4 v[30:33], v30, s[8:9]

; #define GAS __attribute__((address_space(1)))
; #define LAS __attribute__((address_space(3)))
; __device__ __forceinline__ unsigned cvtpk(float lo, float hi) { unsigned r; asm volatile("v_cvt_pk_bf16_f32 %0, %1, %2" : "=v"(r) : "v"(lo), "v"(hi)); return r; }
; __device__ __forceinline__ float bflo(unsigned w) { return __uint_as_float(w << 16); }
; __device__ __forceinline__ float bfhi(unsigned w) { return __uint_as_float(w & 0xffff0000u); }
; __device__ __forceinline__ float siluf(float x) { return x * __builtin_amdgcn_rcpf(1.0f + __expf(-x)); }
; __device__ __forceinline__ void ssd_unit(LAS unsigned char* lds, int b, int h, const bf16* PROJ, const bf16* CONV, const float* dt_bias, const float* a_log, const float* ssd_d,
;                                          bf16* Y, float* SSQ, int tid, int wave, int lane) {
;     ...
;             __builtin_amdgcn_sched_barrier(0);
; #pragma unroll
;             for (int ks = 0; ks < 4; ++ks) { if (2 * ks <= tb) ad = __builtin_amdgcn_mfma_f32_16x16x32_bf16(xfr[ks], mmf[ks], ad, 0, 0, 0);
;                 ao = __builtin_amdgcn_mfma_f32_16x16x32_bf16(sfr[ks], __builtin_bit_cast(bf16x8, (u32x4){clo[ks].x, clo[ks].y, chi[ks].x, chi[ks].y}), ao, 0, 0, 0); }
;             __builtin_amdgcn_sched_barrier(0);
;             const float ea = eac[trow];
;             const u32x2 xv = *(const LAS u32x2*)(lds + C_XB + trow * 128 + (((2 * pb + (q >> 1)) ^ (trow & 7)) << 4) + (q & 1) * 8);
;             const float xx[4] = {bflo(xv.x), bfhi(xv.x), bflo(xv.y), bfhi(xv.y)}, zz[4] = {bflo(zv[j].x), bfhi(zv[j].x), bflo(zv[j].y), bfhi(zv[j].y)};
;             float y[4], sq = 0.f;
; #pragma unroll
;             for (int k = 0; k < 4; ++k) { y[k] = (ad[k] + ea * ao[k] + Dh * xx[k]) * siluf(zz[k]); sq += y[k] * y[k]; }
;             u32x2 ov; ov.x = cvtpk(y[0], y[1]); ov.y = cvtpk(y[2], y[3]);
;             *(GAS u32x2*)(yb + (unsigned)((grow * D_MIX + h * 64 + p0) * 2)) = ov;
;             sq += __shfl_xor(sq, 16); sq += __shfl_xor(sq, 32);
;             if (q == 0) ssqp[pb * 128 + trow] = sq;
;             __builtin_amdgcn_sched_barrier(0);
.LBB0_389:
	s_waitcnt lgkmcnt(2)
	v_add_u32_e32 v126, s93, v197
	v_bitop3_b32 v126, v126, v150, 7 bitop3:0x78
	v_lshlrev_b32_e32 v126, 4, v126
	v_add3_u32 v197, s7, v126, v198
	v_cmp_gt_u32_e64 s[46:47], 16, v150
	s_waitcnt lgkmcnt(0)
	v_mfma_f32_16x16x32_bf16 v[118:121], v[106:109], v[118:121], v[122:125]
	s_nop 2
	v_lshl_add_u32 v122, v200, 2, s88
	ds_read_b32 v126, v122 offset:1536
	s_waitcnt vmcnt(7)
	v_lshlrev_b32_e32 v124, 16, v162
	v_lshl_add_u32 v122, v200, 7, v197
	ds_read_b64 v[122:123], v122
	s_waitcnt lgkmcnt(1)
	v_fma_f32 v114, v118, v126, v114
	v_mul_f32_e32 v118, 0xbfb8aa3b, v124
	v_exp_f32_e32 v118, v118
	s_waitcnt lgkmcnt(0)
	v_lshlrev_b32_e32 v125, 16, v122
	v_fma_f32 v119, v119, v126, v115
	v_and_b32_e32 v115, 0xffff0000, v122
	v_add_f32_e32 v118, 1.0, v118
	v_rcp_f32_e32 v150, v118
	v_fma_f32 v116, v120, v126, v116
	v_fmac_f32_e32 v117, v121, v126
	v_pk_mul_f32 v[124:125], v[150:151], v[124:125]
	s_nop 0
	v_add_f32_e32 v114, v114, v125
	v_mul_f32_e32 v118, v124, v114
	v_and_b32_e32 v114, 0xffff0000, v162
	v_mul_f32_e32 v122, 0xbfb8aa3b, v114
	v_exp_f32_e32 v122, v122
	s_nop 0
	v_add_f32_e32 v122, 1.0, v122
	v_rcp_f32_e32 v150, v122
	s_nop 0
	v_pk_mul_f32 v[114:115], v[150:151], v[114:115]
	s_nop 0
	v_add_f32_e32 v115, v119, v115
	v_mul_f32_e32 v119, v114, v115
	v_lshlrev_b32_e32 v114, 16, v163
	v_mul_f32_e32 v120, 0xbfb8aa3b, v114
	v_exp_f32_e32 v120, v120
	v_lshlrev_b32_e32 v115, 16, v123
	v_mul_f32_e32 v122, v119, v119
	v_fmac_f32_e32 v122, v118, v118
	v_add_f32_e32 v120, 1.0, v120
	v_rcp_f32_e32 v150, v120
	s_nop 0
	v_pk_mul_f32 v[114:115], v[150:151], v[114:115]
	s_nop 0
	v_add_f32_e32 v115, v116, v115
	v_mul_f32_e32 v116, v114, v115
	v_and_b32_e32 v114, 0xffff0000, v163
	v_mul_f32_e32 v120, 0xbfb8aa3b, v114
	v_exp_f32_e32 v120, v120
	v_and_b32_e32 v115, 0xffff0000, v123
	v_fmac_f32_e32 v122, v116, v116
	v_add_f32_e32 v120, 1.0, v120
	v_rcp_f32_e32 v150, v120
	s_nop 0
	v_pk_mul_f32 v[114:115], v[150:151], v[114:115]
	s_nop 0
	v_add_f32_e32 v115, v117, v115
	v_mul_f32_e32 v115, v114, v115
	v_fmac_f32_e32 v122, v115, v115
	v_cvt_pk_bf16_f32 v114, v118, v119
	v_cvt_pk_bf16_f32 v115, v116, v115
	v_lshl_add_u32 v116, v199, 14, v154
	global_store_dwordx2 v116, v[114:115], s[64:65]
	v_and_b32_e32 v115, 64, v175
	v_xor_b32_e32 v114, 16, v175
	v_add_u32_e32 v115, 64, v115
	v_cmp_lt_i32_e32 vcc, v114, v115
	v_xor_b32_e32 v116, 32, v175
	s_nop 0
	v_cndmask_b32_e32 v114, v175, v114, vcc
	v_lshlrev_b32_e32 v163, 2, v114
	ds_bpermute_b32 v114, v163, v122
	v_cmp_lt_i32_e32 vcc, v116, v115
	s_waitcnt lgkmcnt(0)
	v_add_f32_e32 v114, v122, v114
	v_cndmask_b32_e32 v115, v175, v116, vcc
	v_lshlrev_b32_e32 v162, 2, v115
	ds_bpermute_b32 v115, v162, v114
	s_and_saveexec_b64 s[0:1], s[46:47]
	s_cbranch_execz .LBB0_391
	s_waitcnt lgkmcnt(0)
	v_add_f32_e32 v114, v114, v115
	v_lshl_add_u32 v115, v200, 2, s28
	ds_write_b32 v115, v114

; #define GAS __attribute__((address_space(1)))
; #define LAS __attribute__((address_space(3)))
; __device__ __forceinline__ unsigned cvtpk(float lo, float hi) { unsigned r; asm volatile("v_cvt_pk_bf16_f32 %0, %1, %2" : "=v"(r) : "v"(lo), "v"(hi)); return r; }
; __device__ __forceinline__ float bflo(unsigned w) { return __uint_as_float(w << 16); }
; __device__ __forceinline__ float bfhi(unsigned w) { return __uint_as_float(w & 0xffff0000u); }
; __device__ __forceinline__ float siluf(float x) { return x * __builtin_amdgcn_rcpf(1.0f + __expf(-x)); }
; __device__ __forceinline__ void ssd_unit(LAS unsigned char* lds, int b, int h, const bf16* PROJ, const bf16* CONV, const float* dt_bias, const float* a_log, const float* ssd_d,
;                                          bf16* Y, float* SSQ, int tid, int wave, int lane) {
;     ...
;             __builtin_amdgcn_sched_barrier(0);
; #pragma unroll
;             for (int ks = 0; ks < 4; ++ks) { if (2 * ks <= tb) ad = __builtin_amdgcn_mfma_f32_16x16x32_bf16(xfr[ks], mmf[ks], ad, 0, 0, 0);
;                 ao = __builtin_amdgcn_mfma_f32_16x16x32_bf16(sfr[ks], __builtin_bit_cast(bf16x8, (u32x4){clo[ks].x, clo[ks].y, chi[ks].x, chi[ks].y}), ao, 0, 0, 0); }
;             __builtin_amdgcn_sched_barrier(0);
;             const float ea = eac[trow];
;             const u32x2 xv = *(const LAS u32x2*)(lds + C_XB + trow * 128 + (((2 * pb + (q >> 1)) ^ (trow & 7)) << 4) + (q & 1) * 8);
;             const float xx[4] = {bflo(xv.x), bfhi(xv.x), bflo(xv.y), bfhi(xv.y)}, zz[4] = {bflo(zv[j].x), bfhi(zv[j].x), bflo(zv[j].y), bfhi(zv[j].y)};
;             float y[4], sq = 0.f;
; #pragma unroll
;             for (int k = 0; k < 4; ++k) { y[k] = (ad[k] + ea * ao[k] + Dh * xx[k]) * siluf(zz[k]); sq += y[k] * y[k]; }
;             u32x2 ov; ov.x = cvtpk(y[0], y[1]); ov.y = cvtpk(y[2], y[3]);
;             *(GAS u32x2*)(yb + (unsigned)((grow * D_MIX + h * 64 + p0) * 2)) = ov;
;             sq += __shfl_xor(sq, 16); sq += __shfl_xor(sq, 32);
;             if (q == 0) ssqp[pb * 128 + trow] = sq;
;             __builtin_amdgcn_sched_barrier(0);
.LBB0_397:
	s_waitcnt lgkmcnt(2)
	v_add_u32_e32 v128, 16, v199
	s_waitcnt lgkmcnt(0)
	v_mfma_f32_16x16x32_bf16 v[120:123], v[106:109], v[118:121], v[122:125]
	v_add_u32_e32 v118, s29, v181
	v_lshl_add_u32 v119, v118, 2, s88
	ds_read_b32 v119, v119 offset:1600
	v_lshl_add_u32 v124, v150, 7, v197
	s_waitcnt vmcnt(7)
	v_lshlrev_b32_e32 v126, 16, v160
	ds_read_b64 v[124:125], v124
	s_waitcnt lgkmcnt(1)
	v_fma_f32 v114, v120, v119, v114
	v_mul_f32_e32 v120, 0xbfb8aa3b, v126
	v_exp_f32_e32 v120, v120
	s_waitcnt lgkmcnt(0)
	v_lshlrev_b32_e32 v127, 16, v124
	v_fma_f32 v121, v121, v119, v115
	v_and_b32_e32 v115, 0xffff0000, v124
	v_add_f32_e32 v120, 1.0, v120
	v_rcp_f32_e32 v150, v120
	v_fma_f32 v116, v122, v119, v116
	v_fmac_f32_e32 v117, v123, v119
	v_pk_mul_f32 v[126:127], v[150:151], v[126:127]
	s_nop 0
	v_add_f32_e32 v114, v114, v127
	v_mul_f32_e32 v120, v126, v114
	v_and_b32_e32 v114, 0xffff0000, v160
	v_mul_f32_e32 v124, 0xbfb8aa3b, v114
	v_exp_f32_e32 v124, v124
	s_nop 0
	v_add_f32_e32 v124, 1.0, v124
	v_rcp_f32_e32 v150, v124
	s_nop 0
	v_pk_mul_f32 v[114:115], v[150:151], v[114:115]
	s_nop 0
	v_add_f32_e32 v115, v121, v115
	v_mul_f32_e32 v121, v114, v115
	v_lshlrev_b32_e32 v114, 16, v161
	v_mul_f32_e32 v122, 0xbfb8aa3b, v114
	v_exp_f32_e32 v122, v122
	v_lshlrev_b32_e32 v115, 16, v125
	v_mul_f32_e32 v124, v121, v121
	v_fmac_f32_e32 v124, v120, v120
	v_add_f32_e32 v122, 1.0, v122
	v_rcp_f32_e32 v150, v122
	s_nop 0
	v_pk_mul_f32 v[114:115], v[150:151], v[114:115]
	s_nop 0
	v_add_f32_e32 v115, v116, v115
	v_mul_f32_e32 v116, v114, v115
	v_and_b32_e32 v114, 0xffff0000, v161
	v_mul_f32_e32 v119, 0xbfb8aa3b, v114
	v_exp_f32_e32 v119, v119
	v_and_b32_e32 v115, 0xffff0000, v125
	v_fmac_f32_e32 v124, v116, v116
	v_add_f32_e32 v119, 1.0, v119
	v_rcp_f32_e32 v150, v119
	s_nop 0
	v_pk_mul_f32 v[114:115], v[150:151], v[114:115]
	s_nop 0
	v_add_f32_e32 v115, v117, v115
	v_mul_f32_e32 v115, v114, v115
	v_fmac_f32_e32 v124, v115, v115
	v_cvt_pk_bf16_f32 v114, v120, v121
	v_cvt_pk_bf16_f32 v115, v116, v115
	v_lshl_add_u32 v116, v128, 14, v154
	global_store_dwordx2 v116, v[114:115], s[64:65]
	ds_bpermute_b32 v114, v163, v124
	s_waitcnt lgkmcnt(0)
	v_add_f32_e32 v114, v124, v114
	ds_bpermute_b32 v115, v162, v114
	s_and_saveexec_b64 s[0:1], s[46:47]
	s_cbranch_execz .LBB0_399
	s_waitcnt lgkmcnt(0)
	v_add_f32_e32 v114, v114, v115
	v_lshl_add_u32 v115, v118, 2, s28
	ds_write_b32 v115, v114 offset:64

; #define GAS __attribute__((address_space(1)))
; #define LAS __attribute__((address_space(3)))
; __device__ __forceinline__ unsigned cvtpk(float lo, float hi) { unsigned r; asm volatile("v_cvt_pk_bf16_f32 %0, %1, %2" : "=v"(r) : "v"(lo), "v"(hi)); return r; }
; __device__ __forceinline__ float bflo(unsigned w) { return __uint_as_float(w << 16); }
; __device__ __forceinline__ float bfhi(unsigned w) { return __uint_as_float(w & 0xffff0000u); }
; __device__ __forceinline__ float siluf(float x) { return x * __builtin_amdgcn_rcpf(1.0f + __expf(-x)); }
; __device__ __forceinline__ void ssd_unit(LAS unsigned char* lds, int b, int h, const bf16* PROJ, const bf16* CONV, const float* dt_bias, const float* a_log, const float* ssd_d,
;                                          bf16* Y, float* SSQ, int tid, int wave, int lane) {
;     ...
;             __builtin_amdgcn_sched_barrier(0);
; #pragma unroll
;             for (int ks = 0; ks < 4; ++ks) { if (2 * ks <= tb) ad = __builtin_amdgcn_mfma_f32_16x16x32_bf16(xfr[ks], mmf[ks], ad, 0, 0, 0);
;                 ao = __builtin_amdgcn_mfma_f32_16x16x32_bf16(sfr[ks], __builtin_bit_cast(bf16x8, (u32x4){clo[ks].x, clo[ks].y, chi[ks].x, chi[ks].y}), ao, 0, 0, 0); }
;             __builtin_amdgcn_sched_barrier(0);
;             const float ea = eac[trow];
;             const u32x2 xv = *(const LAS u32x2*)(lds + C_XB + trow * 128 + (((2 * pb + (q >> 1)) ^ (trow & 7)) << 4) + (q & 1) * 8);
;             const float xx[4] = {bflo(xv.x), bfhi(xv.x), bflo(xv.y), bfhi(xv.y)}, zz[4] = {bflo(zv[j].x), bfhi(zv[j].x), bflo(zv[j].y), bfhi(zv[j].y)};
;             float y[4], sq = 0.f;
; #pragma unroll
;             for (int k = 0; k < 4; ++k) { y[k] = (ad[k] + ea * ao[k] + Dh * xx[k]) * siluf(zz[k]); sq += y[k] * y[k]; }
;             u32x2 ov; ov.x = cvtpk(y[0], y[1]); ov.y = cvtpk(y[2], y[3]);
;             *(GAS u32x2*)(yb + (unsigned)((grow * D_MIX + h * 64 + p0) * 2)) = ov;
;             sq += __shfl_xor(sq, 16); sq += __shfl_xor(sq, 32);
;             if (q == 0) ssqp[pb * 128 + trow] = sq;
;             __builtin_amdgcn_sched_barrier(0);
.LBB0_403:
	s_waitcnt lgkmcnt(2)
	v_add_u32_e32 v126, 32, v199
	s_waitcnt lgkmcnt(0)
	v_mfma_f32_16x16x32_bf16 v[118:121], v[106:109], v[118:121], v[122:125]
	s_nop 2
	v_lshl_add_u32 v122, v138, 2, s88
	ds_read_b32 v127, v122 offset:1536
	s_waitcnt vmcnt(7)
	v_lshlrev_b32_e32 v124, 16, v158
	v_lshl_add_u32 v122, v138, 7, v197
	ds_read_b64 v[122:123], v122
	s_waitcnt lgkmcnt(1)
	v_fma_f32 v114, v118, v127, v114
	v_mul_f32_e32 v118, 0xbfb8aa3b, v124
	v_exp_f32_e32 v118, v118
	s_waitcnt lgkmcnt(0)
	v_lshlrev_b32_e32 v125, 16, v122
	v_fma_f32 v119, v119, v127, v115
	v_and_b32_e32 v115, 0xffff0000, v122
	v_add_f32_e32 v118, 1.0, v118
	v_rcp_f32_e32 v150, v118
	v_fma_f32 v116, v120, v127, v116
	v_fmac_f32_e32 v117, v121, v127
	v_pk_mul_f32 v[124:125], v[150:151], v[124:125]
	s_nop 0
	v_add_f32_e32 v114, v114, v125
	v_mul_f32_e32 v118, v124, v114
	v_and_b32_e32 v114, 0xffff0000, v158
	v_mul_f32_e32 v122, 0xbfb8aa3b, v114
	v_exp_f32_e32 v122, v122
	s_nop 0
	v_add_f32_e32 v122, 1.0, v122
	v_rcp_f32_e32 v150, v122
	s_nop 0
	v_pk_mul_f32 v[114:115], v[150:151], v[114:115]
	s_nop 0
	v_add_f32_e32 v115, v119, v115
	v_mul_f32_e32 v119, v114, v115
	v_lshlrev_b32_e32 v114, 16, v159
	v_mul_f32_e32 v120, 0xbfb8aa3b, v114
	v_exp_f32_e32 v120, v120
	v_lshlrev_b32_e32 v115, 16, v123
	v_mul_f32_e32 v122, v119, v119
	v_fmac_f32_e32 v122, v118, v118
	v_add_f32_e32 v120, 1.0, v120
	v_rcp_f32_e32 v150, v120
	s_nop 0
	v_pk_mul_f32 v[114:115], v[150:151], v[114:115]
	s_nop 0
	v_add_f32_e32 v115, v116, v115
	v_mul_f32_e32 v116, v114, v115
	v_and_b32_e32 v114, 0xffff0000, v159
	v_mul_f32_e32 v120, 0xbfb8aa3b, v114
	v_exp_f32_e32 v120, v120
	v_and_b32_e32 v115, 0xffff0000, v123
	v_fmac_f32_e32 v122, v116, v116
	v_add_f32_e32 v120, 1.0, v120
	v_rcp_f32_e32 v150, v120
	s_nop 0
	v_pk_mul_f32 v[114:115], v[150:151], v[114:115]
	s_nop 0
	v_add_f32_e32 v115, v117, v115
	v_mul_f32_e32 v115, v114, v115
	v_fmac_f32_e32 v122, v115, v115
	v_cvt_pk_bf16_f32 v114, v118, v119
	v_cvt_pk_bf16_f32 v115, v116, v115
	v_lshl_add_u32 v116, v126, 14, v154
	global_store_dwordx2 v116, v[114:115], s[64:65]
	ds_bpermute_b32 v114, v163, v122
	s_waitcnt lgkmcnt(0)
	v_add_f32_e32 v114, v122, v114
	ds_bpermute_b32 v115, v162, v114
	s_and_saveexec_b64 s[0:1], s[46:47]
	s_cbranch_execz .LBB0_405
	s_waitcnt lgkmcnt(0)
	v_add_f32_e32 v114, v114, v115
	v_lshl_add_u32 v115, v138, 2, s28
	ds_write_b32 v115, v114

; #define GAS __attribute__((address_space(1)))
; #define LAS __attribute__((address_space(3)))
; __device__ __forceinline__ unsigned cvtpk(float lo, float hi) { unsigned r; asm volatile("v_cvt_pk_bf16_f32 %0, %1, %2" : "=v"(r) : "v"(lo), "v"(hi)); return r; }
; __device__ __forceinline__ float bflo(unsigned w) { return __uint_as_float(w << 16); }
; __device__ __forceinline__ float bfhi(unsigned w) { return __uint_as_float(w & 0xffff0000u); }
; __device__ __forceinline__ float siluf(float x) { return x * __builtin_amdgcn_rcpf(1.0f + __expf(-x)); }
; __device__ __forceinline__ void ssd_unit(LAS unsigned char* lds, int b, int h, const bf16* PROJ, const bf16* CONV, const float* dt_bias, const float* a_log, const float* ssd_d,
;                                          bf16* Y, float* SSQ, int tid, int wave, int lane) {
;     ...
;             __builtin_amdgcn_sched_barrier(0);
; #pragma unroll
;             for (int ks = 0; ks < 4; ++ks) { if (2 * ks <= tb) ad = __builtin_amdgcn_mfma_f32_16x16x32_bf16(xfr[ks], mmf[ks], ad, 0, 0, 0);
;                 ao = __builtin_amdgcn_mfma_f32_16x16x32_bf16(sfr[ks], __builtin_bit_cast(bf16x8, (u32x4){clo[ks].x, clo[ks].y, chi[ks].x, chi[ks].y}), ao, 0, 0, 0); }
;             __builtin_amdgcn_sched_barrier(0);
;             const float ea = eac[trow];
;             const u32x2 xv = *(const LAS u32x2*)(lds + C_XB + trow * 128 + (((2 * pb + (q >> 1)) ^ (trow & 7)) << 4) + (q & 1) * 8);
;             const float xx[4] = {bflo(xv.x), bfhi(xv.x), bflo(xv.y), bfhi(xv.y)}, zz[4] = {bflo(zv[j].x), bfhi(zv[j].x), bflo(zv[j].y), bfhi(zv[j].y)};
;             float y[4], sq = 0.f;
; #pragma unroll
;             for (int k = 0; k < 4; ++k) { y[k] = (ad[k] + ea * ao[k] + Dh * xx[k]) * siluf(zz[k]); sq += y[k] * y[k]; }
;             u32x2 ov; ov.x = cvtpk(y[0], y[1]); ov.y = cvtpk(y[2], y[3]);
;             *(GAS u32x2*)(yb + (unsigned)((grow * D_MIX + h * 64 + p0) * 2)) = ov;
;             sq += __shfl_xor(sq, 16); sq += __shfl_xor(sq, 32);
;             if (q == 0) ssqp[pb * 128 + trow] = sq;
;             __builtin_amdgcn_sched_barrier(0);
.LBB0_409:
	s_waitcnt lgkmcnt(0)
	v_mfma_f32_16x16x32_bf16 v[102:105], v[106:109], v[114:117], v[102:105]
	v_lshl_add_u32 v106, v130, 2, s88
	ds_read_b32 v110, v106 offset:1536
	s_waitcnt vmcnt(7)
	v_lshlrev_b32_e32 v108, 16, v156
	v_lshl_add_u32 v106, v130, 7, v197
	ds_read_b64 v[106:107], v106
	s_add_i32 s0, s21, s90
	s_waitcnt lgkmcnt(1)
	v_fma_f32 v98, v102, v110, v98
	v_mul_f32_e32 v102, 0xbfb8aa3b, v108
	v_exp_f32_e32 v102, v102
	s_waitcnt lgkmcnt(0)
	v_lshlrev_b32_e32 v109, 16, v106
	v_fma_f32 v103, v103, v110, v99
	v_and_b32_e32 v99, 0xffff0000, v106
	v_add_f32_e32 v102, 1.0, v102
	v_rcp_f32_e32 v150, v102
	v_fma_f32 v100, v104, v110, v100
	v_fmac_f32_e32 v101, v105, v110
	v_pk_mul_f32 v[108:109], v[150:151], v[108:109]
	s_nop 0
	v_add_f32_e32 v98, v98, v109
	v_mul_f32_e32 v102, v108, v98
	v_and_b32_e32 v98, 0xffff0000, v156
	v_mul_f32_e32 v106, 0xbfb8aa3b, v98
	v_exp_f32_e32 v106, v106
	s_nop 0
	v_add_f32_e32 v106, 1.0, v106
	v_rcp_f32_e32 v150, v106
	s_nop 0
	v_pk_mul_f32 v[98:99], v[150:151], v[98:99]
	s_nop 0
	v_add_f32_e32 v99, v103, v99
	v_mul_f32_e32 v103, v98, v99
	v_lshlrev_b32_e32 v98, 16, v157
	v_mul_f32_e32 v104, 0xbfb8aa3b, v98
	v_exp_f32_e32 v104, v104
	v_lshlrev_b32_e32 v99, 16, v107
	v_mul_f32_e32 v106, v103, v103
	v_fmac_f32_e32 v106, v102, v102
	v_add_f32_e32 v104, 1.0, v104
	v_rcp_f32_e32 v150, v104
	s_nop 0
	v_pk_mul_f32 v[98:99], v[150:151], v[98:99]
	s_nop 0
	v_add_f32_e32 v99, v100, v99
	v_mul_f32_e32 v100, v98, v99
	v_and_b32_e32 v98, 0xffff0000, v157
	v_mul_f32_e32 v104, 0xbfb8aa3b, v98
	v_exp_f32_e32 v104, v104
	v_and_b32_e32 v99, 0xffff0000, v107
	v_fmac_f32_e32 v106, v100, v100
	v_add_f32_e32 v104, 1.0, v104
	v_rcp_f32_e32 v150, v104
	s_nop 0
	v_pk_mul_f32 v[98:99], v[150:151], v[98:99]
	s_nop 0
	v_add_f32_e32 v99, v101, v99
	v_mul_f32_e32 v99, v98, v99
	v_fmac_f32_e32 v106, v99, v99
	v_cvt_pk_bf16_f32 v98, v102, v103
	v_cvt_pk_bf16_f32 v99, v100, v99
	v_add_u32_e32 v100, s0, v181
	v_lshl_add_u32 v100, v100, 14, v154
	global_store_dwordx2 v100, v[98:99], s[64:65]
	ds_bpermute_b32 v98, v163, v106
	s_waitcnt lgkmcnt(0)
	v_add_f32_e32 v98, v106, v98
	ds_bpermute_b32 v99, v162, v98
	s_and_saveexec_b64 s[0:1], s[46:47]
	s_cbranch_execz .LBB0_310
	s_waitcnt lgkmcnt(0)
	v_add_f32_e32 v98, v98, v99
	v_lshl_add_u32 v99, v130, 2, s28
	ds_write_b32 v99, v98
	s_branch .LBB0_310

; __device__ __forceinline__ unsigned cvt_pk_bf16(float lo, float hi) { unsigned r; asm volatile("v_cvt_pk_bf16_f32 %0, %1, %2" : "=v"(r) : "v"(lo), "v"(hi)); return r; }
;     __device__ __forceinline__ void operator()(const f32x4 (&acc)[2][2][4][2], const Unit& u, int wr, int wc, int fr, int fq) const {
;     ...
;             for (int m = 0; m < 4; ++m) { const size_t off = (size_t)(row0 + ai * HALF + m * 16) * ldc + col0;
; #pragma unroll
;                 for (int bj = 0; bj < 2; ++bj) { const f32x4 r0 = __builtin_nontemporal_load((const f32x4*)(R + off + bj * HALF)), r1 = __builtin_nontemporal_load((const f32x4*)(R + off + bj * HALF + 4));
;                     const f32x4 v0 = acc[ai][bj][m][0] + r0, v1 = acc[ai][bj][m][1] + r1;
;                     u32x4 w; w.x = cvt_pk_bf16(v0[0], v0[1]); w.y = cvt_pk_bf16(v0[2], v0[3]); w.z = cvt_pk_bf16(v1[0], v1[1]); w.w = cvt_pk_bf16(v1[2], v1[3]);
;                     __builtin_nontemporal_store(w, (u32x4*)(O + off + bj * HALF)); }
;                 asm volatile("" ::: "memory"); }
.LBB0_566:
	v_lshl_add_u32 v150, s26, 8, v1
	v_lshl_or_b32 v148, s46, 8, v153
	v_lshl_add_u32 v178, v150, 12, v148
	v_lshlrev_b32_e32 v179, 1, v178
	v_lshlrev_b32_e32 v178, 2, v178
	s_andn2_b64 vcc, exec, s[4:5]
	s_mov_b64 s[4:5], -1
	global_load_dwordx4 v[170:173], v178, s[80:81] nt
	global_load_dwordx4 v[174:177], v178, s[80:81] offset:16 nt
	global_load_dwordx4 v[184:187], v178, s[80:81] offset:512 nt
	global_load_dwordx4 v[188:191], v178, s[80:81] offset:528 nt
	v_add_u32_e32 v180, 0x40000, v178
	global_load_dwordx4 v[192:195], v180, s[80:81] nt
	global_load_dwordx4 v[196:199], v180, s[80:81] offset:16 nt
	v_add_u32_e32 v180, 0x40000, v178
	global_load_dwordx4 v[200:203], v180, s[80:81] offset:512 nt
	global_load_dwordx4 v[204:207], v180, s[80:81] offset:528 nt
	v_add_u32_e32 v180, 0x80000, v178
	global_load_dwordx4 v[208:211], v180, s[80:81] nt
	global_load_dwordx4 v[212:215], v180, s[80:81] offset:16 nt
	v_add_u32_e32 v180, 0x80000, v178
	global_load_dwordx4 v[216:219], v180, s[80:81] offset:512 nt
	global_load_dwordx4 v[220:223], v180, s[80:81] offset:528 nt
	v_add_u32_e32 v180, 0xc0000, v178
	global_load_dwordx4 v[224:227], v180, s[80:81] nt
	global_load_dwordx4 v[228:231], v180, s[80:81] offset:16 nt
	v_add_u32_e32 v180, 0xc0000, v178
	global_load_dwordx4 v[232:235], v180, s[80:81] offset:512 nt
	global_load_dwordx4 v[236:239], v180, s[80:81] offset:528 nt
	s_waitcnt vmcnt(14)
	v_pk_add_f32 v[170:171], v[126:127], v[170:171]
	v_pk_add_f32 v[172:173], v[128:129], v[172:173]
	v_pk_add_f32 v[174:175], v[122:123], v[174:175]
	v_pk_add_f32 v[176:177], v[124:125], v[176:177]
	v_cvt_pk_bf16_f32 v122, v170, v171
	v_cvt_pk_bf16_f32 v123, v172, v173
	v_cvt_pk_bf16_f32 v124, v174, v175
	v_cvt_pk_bf16_f32 v125, v176, v177
	global_store_dwordx4 v179, v[122:125], s[6:7] nt
	v_add_u32_e32 v180, 0x200000, v178
	global_load_dwordx4 v[170:173], v180, s[80:81] nt
	global_load_dwordx4 v[174:177], v180, s[80:81] offset:16 nt
	s_waitcnt vmcnt(15)
	v_pk_add_f32 v[184:185], v[118:119], v[184:185]
	v_pk_add_f32 v[186:187], v[120:121], v[186:187]
	v_pk_add_f32 v[188:189], v[114:115], v[188:189]
	v_pk_add_f32 v[190:191], v[116:117], v[190:191]
	v_cvt_pk_bf16_f32 v114, v184, v185
	v_cvt_pk_bf16_f32 v115, v186, v187
	v_cvt_pk_bf16_f32 v116, v188, v189
	v_cvt_pk_bf16_f32 v117, v190, v191
	global_store_dwordx4 v179, v[114:117], s[6:7] offset:256 nt
	v_add_u32_e32 v180, 0x200000, v178
	global_load_dwordx4 v[184:187], v180, s[80:81] offset:512 nt
	global_load_dwordx4 v[188:191], v180, s[80:81] offset:528 nt
	s_waitcnt vmcnt(16)
	v_pk_add_f32 v[192:193], v[110:111], v[192:193]
	v_pk_add_f32 v[194:195], v[112:113], v[194:195]
	v_pk_add_f32 v[196:197], v[106:107], v[196:197]
	v_pk_add_f32 v[198:199], v[108:109], v[198:199]
	v_cvt_pk_bf16_f32 v106, v192, v193
	v_cvt_pk_bf16_f32 v107, v194, v195
	v_cvt_pk_bf16_f32 v108, v196, v197
	v_cvt_pk_bf16_f32 v109, v198, v199
	v_add_u32_e32 v181, 0x20000, v179
	global_store_dwordx4 v181, v[106:109], s[6:7] nt
	v_add_u32_e32 v180, 0x240000, v178
	global_load_dwordx4 v[192:195], v180, s[80:81] nt
	global_load_dwordx4 v[196:199], v180, s[80:81] offset:16 nt
	s_waitcnt vmcnt(17)
	v_pk_add_f32 v[200:201], v[102:103], v[200:201]
	v_pk_add_f32 v[202:203], v[104:105], v[202:203]
	v_pk_add_f32 v[204:205], v[98:99], v[204:205]
	v_pk_add_f32 v[206:207], v[100:101], v[206:207]
	v_cvt_pk_bf16_f32 v98, v200, v201
	v_cvt_pk_bf16_f32 v99, v202, v203
	v_cvt_pk_bf16_f32 v100, v204, v205
	v_cvt_pk_bf16_f32 v101, v206, v207
	v_add_u32_e32 v181, 0x20000, v179
	global_store_dwordx4 v181, v[98:101], s[6:7] offset:256 nt
	v_add_u32_e32 v180, 0x240000, v178
	global_load_dwordx4 v[200:203], v180, s[80:81] offset:512 nt
	global_load_dwordx4 v[204:207], v180, s[80:81] offset:528 nt
	s_waitcnt vmcnt(18)
	v_pk_add_f32 v[208:209], v[94:95], v[208:209]
	v_pk_add_f32 v[210:211], v[96:97], v[210:211]
	v_pk_add_f32 v[212:213], v[90:91], v[212:213]
	v_pk_add_f32 v[214:215], v[92:93], v[214:215]
	v_cvt_pk_bf16_f32 v90, v208, v209
	v_cvt_pk_bf16_f32 v91, v210, v211
	v_cvt_pk_bf16_f32 v92, v212, v213
	v_cvt_pk_bf16_f32 v93, v214, v215
	v_add_u32_e32 v181, 0x40000, v179
	global_store_dwordx4 v181, v[90:93], s[6:7] nt
	v_add_u32_e32 v180, 0x280000, v178
	global_load_dwordx4 v[208:211], v180, s[80:81] nt
	global_load_dwordx4 v[212:215], v180, s[80:81] offset:16 nt
	s_waitcnt vmcnt(19)
	v_pk_add_f32 v[216:217], v[86:87], v[216:217]
	v_pk_add_f32 v[218:219], v[88:89], v[218:219]
	v_pk_add_f32 v[220:221], v[82:83], v[220:221]
	v_pk_add_f32 v[222:223], v[84:85], v[222:223]
	v_cvt_pk_bf16_f32 v82, v216, v217
	v_cvt_pk_bf16_f32 v83, v218, v219
	v_cvt_pk_bf16_f32 v84, v220, v221
	v_cvt_pk_bf16_f32 v85, v222, v223
	v_add_u32_e32 v181, 0x40000, v179
	global_store_dwordx4 v181, v[82:85], s[6:7] offset:256 nt
	v_add_u32_e32 v180, 0x280000, v178
	global_load_dwordx4 v[216:219], v180, s[80:81] offset:512 nt
	global_load_dwordx4 v[220:223], v180, s[80:81] offset:528 nt
	s_waitcnt vmcnt(20)
; __device__ __forceinline__ unsigned cvt_pk_bf16(float lo, float hi) { unsigned r; asm volatile("v_cvt_pk_bf16_f32 %0, %1, %2" : "=v"(r) : "v"(lo), "v"(hi)); return r; }
;     __device__ __forceinline__ void operator()(const f32x4 (&acc)[2][2][4][2], const Unit& u, int wr, int wc, int fr, int fq) const {
;     ...
;             for (int m = 0; m < 4; ++m) { const size_t off = (size_t)(row0 + ai * HALF + m * 16) * ldc + col0;
; #pragma unroll
;                 for (int bj = 0; bj < 2; ++bj) { const f32x4 r0 = __builtin_nontemporal_load((const f32x4*)(R + off + bj * HALF)), r1 = __builtin_nontemporal_load((const f32x4*)(R + off + bj * HALF + 4));
;                     const f32x4 v0 = acc[ai][bj][m][0] + r0, v1 = acc[ai][bj][m][1] + r1;
;                     u32x4 w; w.x = cvt_pk_bf16(v0[0], v0[1]); w.y = cvt_pk_bf16(v0[2], v0[3]); w.z = cvt_pk_bf16(v1[0], v1[1]); w.w = cvt_pk_bf16(v1[2], v1[3]);
;                     __builtin_nontemporal_store(w, (u32x4*)(O + off + bj * HALF)); }
;                 asm volatile("" ::: "memory"); }
	v_pk_add_f32 v[224:225], v[78:79], v[224:225]
	v_pk_add_f32 v[226:227], v[80:81], v[226:227]
	v_pk_add_f32 v[228:229], v[74:75], v[228:229]
	v_pk_add_f32 v[230:231], v[76:77], v[230:231]
	v_cvt_pk_bf16_f32 v74, v224, v225
	v_cvt_pk_bf16_f32 v75, v226, v227
	v_cvt_pk_bf16_f32 v76, v228, v229
	v_cvt_pk_bf16_f32 v77, v230, v231
	v_add_u32_e32 v181, 0x60000, v179
	global_store_dwordx4 v181, v[74:77], s[6:7] nt
	v_add_u32_e32 v180, 0x2c0000, v178
	global_load_dwordx4 v[224:227], v180, s[80:81] nt
	global_load_dwordx4 v[228:231], v180, s[80:81] offset:16 nt
	s_waitcnt vmcnt(21)
	v_pk_add_f32 v[232:233], v[70:71], v[232:233]
	v_pk_add_f32 v[234:235], v[72:73], v[234:235]
	v_pk_add_f32 v[236:237], v[66:67], v[236:237]
	v_pk_add_f32 v[238:239], v[68:69], v[238:239]
	v_cvt_pk_bf16_f32 v66, v232, v233
	v_cvt_pk_bf16_f32 v67, v234, v235
	v_cvt_pk_bf16_f32 v68, v236, v237
	v_cvt_pk_bf16_f32 v69, v238, v239
	v_add_u32_e32 v181, 0x60000, v179
	global_store_dwordx4 v181, v[66:69], s[6:7] offset:256 nt
	v_add_u32_e32 v180, 0x2c0000, v178
	global_load_dwordx4 v[232:235], v180, s[80:81] offset:512 nt
	global_load_dwordx4 v[236:239], v180, s[80:81] offset:528 nt
	s_waitcnt vmcnt(21)
	v_pk_add_f32 v[170:171], v[62:63], v[170:171]
	v_pk_add_f32 v[172:173], v[64:65], v[172:173]
	v_pk_add_f32 v[174:175], v[58:59], v[174:175]
	v_pk_add_f32 v[176:177], v[60:61], v[176:177]
	v_cvt_pk_bf16_f32 v58, v170, v171
	v_cvt_pk_bf16_f32 v59, v172, v173
	v_cvt_pk_bf16_f32 v60, v174, v175
	v_cvt_pk_bf16_f32 v61, v176, v177
	v_add_u32_e32 v181, 0x100000, v179
	global_store_dwordx4 v181, v[58:61], s[6:7] nt
	s_waitcnt vmcnt(19)
	v_pk_add_f32 v[184:185], v[54:55], v[184:185]
	v_pk_add_f32 v[186:187], v[56:57], v[186:187]
	v_pk_add_f32 v[188:189], v[50:51], v[188:189]
	v_pk_add_f32 v[190:191], v[52:53], v[190:191]
	v_cvt_pk_bf16_f32 v50, v184, v185
	v_cvt_pk_bf16_f32 v51, v186, v187
	v_cvt_pk_bf16_f32 v52, v188, v189
	v_cvt_pk_bf16_f32 v53, v190, v191
	v_add_u32_e32 v181, 0x100000, v179
	global_store_dwordx4 v181, v[50:53], s[6:7] offset:256 nt
	s_waitcnt vmcnt(17)
	v_pk_add_f32 v[192:193], v[46:47], v[192:193]
	v_pk_add_f32 v[194:195], v[48:49], v[194:195]
	v_pk_add_f32 v[196:197], v[42:43], v[196:197]
	v_pk_add_f32 v[198:199], v[44:45], v[198:199]
	v_cvt_pk_bf16_f32 v42, v192, v193
	v_cvt_pk_bf16_f32 v43, v194, v195
	v_cvt_pk_bf16_f32 v44, v196, v197
	v_cvt_pk_bf16_f32 v45, v198, v199
	v_add_u32_e32 v181, 0x120000, v179
	global_store_dwordx4 v181, v[42:45], s[6:7] nt
	s_waitcnt vmcnt(15)
	v_pk_add_f32 v[200:201], v[38:39], v[200:201]
	v_pk_add_f32 v[202:203], v[40:41], v[202:203]
	v_pk_add_f32 v[204:205], v[34:35], v[204:205]
	v_pk_add_f32 v[206:207], v[36:37], v[206:207]
	v_cvt_pk_bf16_f32 v34, v200, v201
	v_cvt_pk_bf16_f32 v35, v202, v203
	v_cvt_pk_bf16_f32 v36, v204, v205
	v_cvt_pk_bf16_f32 v37, v206, v207
	v_add_u32_e32 v181, 0x120000, v179
	global_store_dwordx4 v181, v[34:37], s[6:7] offset:256 nt
	s_waitcnt vmcnt(13)
	v_pk_add_f32 v[208:209], v[30:31], v[208:209]
	v_pk_add_f32 v[210:211], v[32:33], v[210:211]
	v_pk_add_f32 v[212:213], v[26:27], v[212:213]
	v_pk_add_f32 v[214:215], v[28:29], v[214:215]
	v_cvt_pk_bf16_f32 v26, v208, v209
	v_cvt_pk_bf16_f32 v27, v210, v211
	v_cvt_pk_bf16_f32 v28, v212, v213
	v_cvt_pk_bf16_f32 v29, v214, v215
	v_add_u32_e32 v181, 0x140000, v179
	global_store_dwordx4 v181, v[26:29], s[6:7] nt
	s_waitcnt vmcnt(11)
	v_pk_add_f32 v[216:217], v[22:23], v[216:217]
	v_pk_add_f32 v[218:219], v[24:25], v[218:219]
	v_pk_add_f32 v[220:221], v[18:19], v[220:221]
	v_pk_add_f32 v[222:223], v[20:21], v[222:223]
	v_cvt_pk_bf16_f32 v18, v216, v217
	v_cvt_pk_bf16_f32 v19, v218, v219
	v_cvt_pk_bf16_f32 v20, v220, v221
	v_cvt_pk_bf16_f32 v21, v222, v223
	v_add_u32_e32 v181, 0x140000, v179
	global_store_dwordx4 v181, v[18:21], s[6:7] offset:256 nt
	s_waitcnt vmcnt(9)
	v_pk_add_f32 v[224:225], v[14:15], v[224:225]
	v_pk_add_f32 v[226:227], v[16:17], v[226:227]
	v_pk_add_f32 v[228:229], v[10:11], v[228:229]
	v_pk_add_f32 v[230:231], v[12:13], v[230:231]
	v_cvt_pk_bf16_f32 v10, v224, v225
	v_cvt_pk_bf16_f32 v11, v226, v227
	v_cvt_pk_bf16_f32 v12, v228, v229
	v_cvt_pk_bf16_f32 v13, v230, v231
	v_add_u32_e32 v181, 0x160000, v179
	global_store_dwordx4 v181, v[10:13], s[6:7] nt
	s_waitcnt vmcnt(7)
	v_pk_add_f32 v[232:233], v[6:7], v[232:233]
	v_pk_add_f32 v[234:235], v[8:9], v[234:235]
	v_pk_add_f32 v[236:237], v[2:3], v[236:237]
	v_pk_add_f32 v[238:239], v[4:5], v[238:239]
	v_cvt_pk_bf16_f32 v2, v232, v233
	v_cvt_pk_bf16_f32 v3, v234, v235
	v_cvt_pk_bf16_f32 v4, v236, v237
	v_cvt_pk_bf16_f32 v5, v238, v239
	v_add_u32_e32 v181, 0x160000, v179
	global_store_dwordx4 v181, v[2:5], s[6:7] offset:256 nt
	s_cbranch_vccnz .LBB0_555
	s_andn2_b64 vcc, exec, s[0:1]
	s_cbranch_vccnz .LBB0_554
	s_barrier
	s_branch .LBB0_554

;     __device__ __forceinline__ void operator()(const f32x4 (&acc)[2][2][4][2], const Unit& u, int wr, int wc, int fr, int fq) const {
;     ...
;             for (int m = 0; m < 4; ++m) { const int row = row0 + ai * HALF + m * 16; const float rsv = rowscale[row]; const size_t off = (size_t)row * ldc + col0;
; #pragma unroll
;                 for (int bj = 0; bj < 2; ++bj)
; #pragma unroll
;                     for (int n = 0; n < 2; ++n) __builtin_nontemporal_store(acc[ai][bj][m][n] * rsv, (f32x4*)(C + off + bj * HALF + n * 16)); }
.LBB0_710:
	v_lshl_add_u32 v154, s0, 8, v148
	v_ashrrev_i32_e32 v155, 31, v154
	v_lshl_add_u64 v[142:143], v[154:155], 2, s[10:11]
	global_load_dword v184, v[142:143], off
	global_load_dword v186, v[142:143], off offset:64
	global_load_dword v188, v[142:143], off offset:128
	global_load_dword v190, v[142:143], off offset:192
	global_load_dword v192, v[142:143], off offset:512
	global_load_dword v194, v[142:143], off offset:576
	global_load_dword v196, v[142:143], off offset:640
	global_load_dword v198, v[142:143], off offset:704
	v_lshl_or_b32 v144, s1, 8, v150
	v_ashrrev_i32_e32 v145, 31, v144
	v_lshlrev_b64 v[160:161], 13, v[154:155]
	v_or_b32_e32 v158, 16, v154
	v_lshlrev_b64 v[162:163], 2, v[144:145]
	v_lshl_add_u64 v[144:145], s[40:41], 0, v[160:161]
	v_ashrrev_i32_e32 v159, 31, v158
	v_lshl_add_u64 v[144:145], v[144:145], 0, v[162:163]
	v_lshl_add_u64 v[160:161], v[158:159], 2, s[10:11]
	s_waitcnt vmcnt(0)
	v_pk_mul_f32 v[128:129], v[128:129], v[184:185] op_sel_hi:[1,0]
	v_pk_mul_f32 v[126:127], v[126:127], v[184:185] op_sel_hi:[1,0]
	v_pk_mul_f32 v[124:125], v[124:125], v[184:185] op_sel_hi:[1,0]
	v_pk_mul_f32 v[122:123], v[122:123], v[184:185] op_sel_hi:[1,0]
	v_pk_mul_f32 v[120:121], v[120:121], v[184:185] op_sel_hi:[1,0]
	v_pk_mul_f32 v[118:119], v[118:119], v[184:185] op_sel_hi:[1,0]
	v_pk_mul_f32 v[116:117], v[116:117], v[184:185] op_sel_hi:[1,0]
	v_pk_mul_f32 v[114:115], v[114:115], v[184:185] op_sel_hi:[1,0]
	global_store_dwordx4 v[144:145], v[126:129], off nt
	global_store_dwordx4 v[144:145], v[122:125], off offset:64 nt
	global_store_dwordx4 v[144:145], v[118:121], off offset:512 nt
	global_store_dwordx4 v[144:145], v[114:117], off offset:576 nt
	s_nop 3
	v_lshlrev_b64 v[118:119], 13, v[158:159]
	v_or_b32_e32 v116, 32, v154
	v_lshl_add_u64 v[118:119], s[40:41], 0, v[118:119]
	v_ashrrev_i32_e32 v117, 31, v116
	v_lshl_add_u64 v[118:119], v[118:119], 0, v[162:163]
	v_lshl_add_u64 v[120:121], v[116:117], 2, s[10:11]
	s_nop 3
	v_pk_mul_f32 v[112:113], v[112:113], v[186:187] op_sel_hi:[1,0]
	v_pk_mul_f32 v[110:111], v[110:111], v[186:187] op_sel_hi:[1,0]
	v_pk_mul_f32 v[108:109], v[108:109], v[186:187] op_sel_hi:[1,0]
	v_pk_mul_f32 v[106:107], v[106:107], v[186:187] op_sel_hi:[1,0]
	v_pk_mul_f32 v[104:105], v[104:105], v[186:187] op_sel_hi:[1,0]
	v_pk_mul_f32 v[102:103], v[102:103], v[186:187] op_sel_hi:[1,0]
	v_pk_mul_f32 v[100:101], v[100:101], v[186:187] op_sel_hi:[1,0]
	v_pk_mul_f32 v[98:99], v[98:99], v[186:187] op_sel_hi:[1,0]
	global_store_dwordx4 v[118:119], v[110:113], off nt
	global_store_dwordx4 v[118:119], v[106:109], off offset:64 nt
	global_store_dwordx4 v[118:119], v[102:105], off offset:512 nt
	global_store_dwordx4 v[118:119], v[98:101], off offset:576 nt
	s_nop 3
	v_lshlrev_b64 v[102:103], 13, v[116:117]
	v_or_b32_e32 v100, 48, v154
	v_lshl_add_u64 v[102:103], s[40:41], 0, v[102:103]
	v_ashrrev_i32_e32 v101, 31, v100
	v_lshl_add_u64 v[102:103], v[102:103], 0, v[162:163]
	v_lshl_add_u64 v[104:105], v[100:101], 2, s[10:11]
	s_nop 3
	v_pk_mul_f32 v[96:97], v[96:97], v[188:189] op_sel_hi:[1,0]
	v_pk_mul_f32 v[94:95], v[94:95], v[188:189] op_sel_hi:[1,0]
	v_pk_mul_f32 v[92:93], v[92:93], v[188:189] op_sel_hi:[1,0]
	v_pk_mul_f32 v[90:91], v[90:91], v[188:189] op_sel_hi:[1,0]
	v_pk_mul_f32 v[84:85], v[84:85], v[188:189] op_sel_hi:[1,0]
	v_pk_mul_f32 v[82:83], v[82:83], v[188:189] op_sel_hi:[1,0]
	v_pk_mul_f32 v[76:77], v[76:77], v[188:189] op_sel_hi:[1,0]
	v_pk_mul_f32 v[74:75], v[74:75], v[188:189] op_sel_hi:[1,0]
	global_store_dwordx4 v[102:103], v[94:97], off nt
	global_store_dwordx4 v[102:103], v[90:93], off offset:64 nt
	global_store_dwordx4 v[102:103], v[82:85], off offset:512 nt
	global_store_dwordx4 v[102:103], v[74:77], off offset:576 nt
	s_nop 3
	s_nop 3
	v_pk_mul_f32 v[80:81], v[80:81], v[190:191] op_sel_hi:[1,0]
	v_lshlrev_b64 v[74:75], 13, v[100:101]
	v_lshl_add_u64 v[74:75], s[40:41], 0, v[74:75]
	v_lshl_add_u64 v[84:85], v[74:75], 0, v[162:163]
	v_pk_mul_f32 v[76:77], v[88:89], v[190:191] op_sel_hi:[1,0]
	v_pk_mul_f32 v[74:75], v[86:87], v[190:191] op_sel_hi:[1,0]
	v_pk_mul_f32 v[78:79], v[78:79], v[190:191] op_sel_hi:[1,0]
;     __device__ __forceinline__ void operator()(const f32x4 (&acc)[2][2][4][2], const Unit& u, int wr, int wc, int fr, int fq) const {
;     ...
;             for (int m = 0; m < 4; ++m) { const int row = row0 + ai * HALF + m * 16; const float rsv = rowscale[row]; const size_t off = (size_t)row * ldc + col0;
; #pragma unroll
;                 for (int bj = 0; bj < 2; ++bj)
; #pragma unroll
;                     for (int n = 0; n < 2; ++n) __builtin_nontemporal_store(acc[ai][bj][m][n] * rsv, (f32x4*)(C + off + bj * HALF + n * 16)); }
	v_pk_mul_f32 v[72:73], v[72:73], v[190:191] op_sel_hi:[1,0]
	v_pk_mul_f32 v[70:71], v[70:71], v[190:191] op_sel_hi:[1,0]
	v_pk_mul_f32 v[68:69], v[68:69], v[190:191] op_sel_hi:[1,0]
	v_pk_mul_f32 v[66:67], v[66:67], v[190:191] op_sel_hi:[1,0]
	global_store_dwordx4 v[84:85], v[74:77], off nt
	global_store_dwordx4 v[84:85], v[78:81], off offset:64 nt
	global_store_dwordx4 v[84:85], v[70:73], off offset:512 nt
	global_store_dwordx4 v[84:85], v[66:69], off offset:576 nt
	s_nop 3
	v_add_co_u32_e32 v70, vcc, s53, v144
	v_lshl_add_u64 v[68:69], v[144:145], 0, s[2:3]
	s_nop 0
	v_addc_co_u32_e32 v71, vcc, 0, v145, vcc
	s_nop 3
	v_pk_mul_f32 v[64:65], v[64:65], v[192:193] op_sel_hi:[1,0]
	v_pk_mul_f32 v[62:63], v[62:63], v[192:193] op_sel_hi:[1,0]
	v_pk_mul_f32 v[60:61], v[60:61], v[192:193] op_sel_hi:[1,0]
	v_pk_mul_f32 v[58:59], v[58:59], v[192:193] op_sel_hi:[1,0]
	v_pk_mul_f32 v[56:57], v[56:57], v[192:193] op_sel_hi:[1,0]
	v_pk_mul_f32 v[54:55], v[54:55], v[192:193] op_sel_hi:[1,0]
	v_pk_mul_f32 v[48:49], v[48:49], v[192:193] op_sel_hi:[1,0]
	v_pk_mul_f32 v[46:47], v[46:47], v[192:193] op_sel_hi:[1,0]
	global_store_dwordx4 v[70:71], v[62:65], off nt
	global_store_dwordx4 v[68:69], v[58:61], off offset:64 nt
	global_store_dwordx4 v[68:69], v[54:57], off offset:512 nt
	global_store_dwordx4 v[68:69], v[46:49], off offset:576 nt
	s_nop 3
	v_add_co_u32_e32 v58, vcc, s54, v144
	v_lshl_add_u64 v[56:57], v[144:145], 0, s[16:17]
	s_nop 0
	v_addc_co_u32_e32 v59, vcc, 0, v145, vcc
	s_nop 3
	v_pk_mul_f32 v[48:49], v[52:53], v[194:195] op_sel_hi:[1,0]
	v_pk_mul_f32 v[46:47], v[50:51], v[194:195] op_sel_hi:[1,0]
	v_pk_mul_f32 v[44:45], v[44:45], v[194:195] op_sel_hi:[1,0]
	v_pk_mul_f32 v[42:43], v[42:43], v[194:195] op_sel_hi:[1,0]
	v_pk_mul_f32 v[40:41], v[40:41], v[194:195] op_sel_hi:[1,0]
	v_pk_mul_f32 v[38:39], v[38:39], v[194:195] op_sel_hi:[1,0]
	v_pk_mul_f32 v[32:33], v[32:33], v[194:195] op_sel_hi:[1,0]
	v_pk_mul_f32 v[30:31], v[30:31], v[194:195] op_sel_hi:[1,0]
	global_store_dwordx4 v[58:59], v[46:49], off nt
	global_store_dwordx4 v[56:57], v[42:45], off offset:64 nt
	global_store_dwordx4 v[56:57], v[38:41], off offset:512 nt
	global_store_dwordx4 v[56:57], v[30:33], off offset:576 nt
	s_nop 3
	v_add_co_u32_e32 v42, vcc, s55, v144
	v_lshl_add_u64 v[40:41], v[144:145], 0, s[18:19]
	s_nop 0
	v_addc_co_u32_e32 v43, vcc, 0, v145, vcc
	s_andn2_b64 vcc, exec, s[4:5]
	s_nop 3
	v_pk_mul_f32 v[32:33], v[36:37], v[196:197] op_sel_hi:[1,0]
	v_pk_mul_f32 v[30:31], v[34:35], v[196:197] op_sel_hi:[1,0]
	v_pk_mul_f32 v[28:29], v[28:29], v[196:197] op_sel_hi:[1,0]
	v_pk_mul_f32 v[26:27], v[26:27], v[196:197] op_sel_hi:[1,0]
	v_pk_mul_f32 v[24:25], v[24:25], v[196:197] op_sel_hi:[1,0]
	v_pk_mul_f32 v[22:23], v[22:23], v[196:197] op_sel_hi:[1,0]
	v_pk_mul_f32 v[20:21], v[20:21], v[196:197] op_sel_hi:[1,0]
	v_pk_mul_f32 v[18:19], v[18:19], v[196:197] op_sel_hi:[1,0]
	global_store_dwordx4 v[42:43], v[30:33], off nt
	global_store_dwordx4 v[40:41], v[26:29], off offset:64 nt
	global_store_dwordx4 v[40:41], v[22:25], off offset:512 nt
	global_store_dwordx4 v[40:41], v[18:21], off offset:576 nt
	s_nop 3
	v_add_co_u32_e64 v22, s[0:1], s56, v144
	v_lshl_add_u64 v[20:21], v[144:145], 0, s[20:21]
	s_nop 0
	v_addc_co_u32_e64 v23, s[0:1], 0, v145, s[0:1]
	s_mov_b64 s[0:1], -1
	s_nop 3
	v_pk_mul_f32 v[16:17], v[16:17], v[198:199] op_sel_hi:[1,0]
	v_pk_mul_f32 v[14:15], v[14:15], v[198:199] op_sel_hi:[1,0]
	v_pk_mul_f32 v[12:13], v[12:13], v[198:199] op_sel_hi:[1,0]
	v_pk_mul_f32 v[10:11], v[10:11], v[198:199] op_sel_hi:[1,0]
	v_pk_mul_f32 v[8:9], v[8:9], v[198:199] op_sel_hi:[1,0]
	v_pk_mul_f32 v[6:7], v[6:7], v[198:199] op_sel_hi:[1,0]
	v_pk_mul_f32 v[4:5], v[4:5], v[198:199] op_sel_hi:[1,0]
	v_pk_mul_f32 v[2:3], v[2:3], v[198:199] op_sel_hi:[1,0]
	global_store_dwordx4 v[22:23], v[14:17], off nt
	global_store_dwordx4 v[20:21], v[10:13], off offset:64 nt
	global_store_dwordx4 v[20:21], v[6:9], off offset:512 nt
	global_store_dwordx4 v[20:21], v[2:5], off offset:576 nt
	s_cbranch_vccnz .LBB0_699
	s_andn2_b64 vcc, exec, s[8:9]
	s_cbranch_vccnz .LBB0_698
	s_barrier
	s_branch .LBB0_698
